# non-temporal loads for the modulation weights (prologue) and the layer-0 f32 activations (both read once from HBM)
# baseline (speedup 1.0000x reference)
.LBB0_25:
	v_add_co_u32_e32 v38, vcc, s0, v26
	global_load_dword v70, v[26:27], off nt
	s_nop 0
	v_addc_co_u32_e32 v39, vcc, 0, v27, vcc
	global_load_dword v72, v[38:39], off nt
	v_add_u32_e32 v37, s18, v32
	ds_read2st64_b64 v[38:41], v37 offset1:8
	ds_read2st64_b64 v[42:45], v37 offset0:16 offset1:24
	ds_read2st64_b64 v[46:49], v37 offset0:32 offset1:40
	ds_read2st64_b64 v[50:53], v37 offset0:48 offset1:56
	ds_read2st64_b64 v[54:57], v37 offset0:64 offset1:72
	ds_read2st64_b64 v[58:61], v37 offset0:80 offset1:88
	ds_read2st64_b64 v[62:65], v37 offset0:96 offset1:104
	ds_read2st64_b64 v[66:69], v37 offset0:112 offset1:120
	v_add_u32_e32 v37, 0x10000, v37
	ds_read_b64 v[74:75], v37
	s_waitcnt lgkmcnt(8)
	v_mov_b32_e32 v76, v38
	v_mov_b32_e32 v77, v40
	s_waitcnt lgkmcnt(7)
	v_mov_b32_e32 v78, v42
	v_mov_b32_e32 v79, v44
	s_waitcnt lgkmcnt(6)
	v_mov_b32_e32 v80, v46
	v_mov_b32_e32 v81, v48
	s_waitcnt lgkmcnt(5)
	v_mov_b32_e32 v82, v50
	v_mov_b32_e32 v83, v52
	s_waitcnt lgkmcnt(4)
	v_mov_b32_e32 v84, v54
	v_mov_b32_e32 v85, v56
	s_waitcnt lgkmcnt(3)
	v_mov_b32_e32 v86, v58
	v_mov_b32_e32 v87, v60
	s_waitcnt lgkmcnt(2)
	v_mov_b32_e32 v88, v62
	v_mov_b32_e32 v89, v64
	s_waitcnt lgkmcnt(1)
	v_mov_b32_e32 v90, v66
	v_mov_b32_e32 v91, v68
	s_add_i32 s18, s18, 8
	v_mov_b32_e32 v40, v39
	v_mov_b32_e32 v44, v43
	v_mov_b32_e32 v48, v47
	v_mov_b32_e32 v52, v51
	v_mov_b32_e32 v56, v55
	v_mov_b32_e32 v60, v59
	v_mov_b32_e32 v64, v63
	v_mov_b32_e32 v68, v67
	v_lshl_add_u64 v[26:27], v[26:27], 0, s[34:35]
	s_cmpk_eq_i32 s18, 0x800
	s_waitcnt vmcnt(1)
	v_pk_fma_f32 v[20:21], v[70:71], v[76:77], v[20:21] op_sel_hi:[0,1,1]
	v_pk_fma_f32 v[22:23], v[70:71], v[78:79], v[22:23] op_sel_hi:[0,1,1]
	v_pk_fma_f32 v[14:15], v[70:71], v[80:81], v[14:15] op_sel_hi:[0,1,1]
	v_pk_fma_f32 v[16:17], v[70:71], v[82:83], v[16:17] op_sel_hi:[0,1,1]
	v_pk_fma_f32 v[18:19], v[70:71], v[84:85], v[18:19] op_sel_hi:[0,1,1]
	v_pk_fma_f32 v[12:13], v[70:71], v[86:87], v[12:13] op_sel_hi:[0,1,1]
	v_pk_fma_f32 v[10:11], v[70:71], v[88:89], v[10:11] op_sel_hi:[0,1,1]
	v_pk_fma_f32 v[8:9], v[70:71], v[90:91], v[8:9] op_sel_hi:[0,1,1]
	s_waitcnt lgkmcnt(0)
	v_fmac_f32_e32 v4, v70, v74
	s_waitcnt vmcnt(0)
	v_pk_fma_f32 v[20:21], v[72:73], v[40:41], v[20:21] op_sel_hi:[0,1,1]
	v_pk_fma_f32 v[22:23], v[72:73], v[44:45], v[22:23] op_sel_hi:[0,1,1]
	v_pk_fma_f32 v[14:15], v[72:73], v[48:49], v[14:15] op_sel_hi:[0,1,1]
	v_pk_fma_f32 v[16:17], v[72:73], v[52:53], v[16:17] op_sel_hi:[0,1,1]
	v_pk_fma_f32 v[18:19], v[72:73], v[56:57], v[18:19] op_sel_hi:[0,1,1]
	v_pk_fma_f32 v[12:13], v[72:73], v[60:61], v[12:13] op_sel_hi:[0,1,1]
	v_pk_fma_f32 v[10:11], v[72:73], v[64:65], v[10:11] op_sel_hi:[0,1,1]
	v_pk_fma_f32 v[8:9], v[72:73], v[68:69], v[8:9] op_sel_hi:[0,1,1]
	v_fmac_f32_e32 v4, v72, v75
	s_cbranch_scc0 .LBB0_25
	v_add_u32_e32 v26, 0x11000, v35
	s_and_saveexec_b64 s[18:19], s[6:7]
	s_cbranch_execz .LBB0_28
	ds_write2_b32 v26, v20, v21 offset1:1
	ds_write2_b32 v26, v22, v23 offset0:2 offset1:3
	ds_write2_b32 v26, v14, v15 offset0:4 offset1:5
	ds_write2_b32 v26, v16, v17 offset0:6 offset1:7
	ds_write2_b32 v26, v18, v19 offset0:8 offset1:9
	ds_write2_b32 v26, v12, v13 offset0:10 offset1:11
	ds_write2_b32 v26, v10, v11 offset0:12 offset1:13
	ds_write2_b32 v26, v8, v9 offset0:14 offset1:15
	ds_write_b32 v26, v4 offset:64

.LBB0_330:
	v_ashrrev_i32_e32 v3, 31, v2
	v_lshlrev_b64 v[2:3], 12, v[2:3]
	v_lshl_add_u64 v[2:3], s[74:75], 0, v[2:3]
	v_lshl_add_u64 v[2:3], v[2:3], 0, v[130:131]
	global_load_dwordx4 v[14:17], v[2:3], off nt
	global_load_dwordx4 v[10:13], v[2:3], off offset:1024 nt
	global_load_dwordx4 v[6:9], v[2:3], off offset:2048 nt
	s_nop 0
	global_load_dwordx4 v[2:5], v[2:3], off offset:3072 nt
	v_add_u32_e32 v60, 8, v40
	s_waitcnt vmcnt(5)
	v_mov_b32_e32 v61, v37
	s_waitcnt vmcnt(4)
	v_mov_b32_e32 v72, v39
	v_mov_b64_e32 v[48:49], v[56:57]
	v_mov_b64_e32 v[46:47], v[54:55]
	v_mov_b64_e32 v[44:45], v[52:53]
	v_mov_b64_e32 v[42:43], v[50:51]
